# LN1 pass-1 to pass-2 hand-over: two partial drains of the wave's own stores ahead of plain VALU setup removed (no load outstanding there)
# baseline (speedup 1.0000x reference)
.LBB0_3231:
	v_readlane_b32 s38, v253, 0
	s_waitcnt vmcnt(63) expcnt(7) lgkmcnt(15)
	s_barrier
	s_cmpk_gt_i32 s38, 0x1ff
	s_cbranch_scc1 .LBB0_3269
	s_add_u32 s16, s2, 0x202b0000
	s_addc_u32 s17, s3, 0
	s_add_u32 s18, s2, 0x202c0000
	s_addc_u32 s19, s3, 0
	s_add_u32 s20, s2, 0x202d0000
	s_addc_u32 s21, s3, 0
	s_add_u32 s22, s2, 0x203d0000
	s_addc_u32 s23, s3, 0
	v_readlane_b32 s8, v254, 1
	s_add_u32 s24, s2, 0x203e0000
	s_mul_i32 s64, s8, 0x6000
	s_addc_u32 s25, s3, 0
	s_lshl_b64 s[4:5], s[64:65], 4
	s_add_u32 s6, s2, s4
	s_addc_u32 s7, s3, s5
	s_lshl_b32 s64, s8, 2
	s_lshl_b64 s[4:5], s[64:65], 2
	s_add_u32 s26, s12, s4
	s_addc_u32 s27, s10, s5
	s_lshl_b32 s64, s8, 5
	s_lshl_b64 s[4:5], s[64:65], 2
	s_add_u32 s28, s13, s4
	s_addc_u32 s29, s11, s5
	s_lshl_b32 s64, s8, 10
	s_lshl_b64 s[4:5], s[64:65], 2
	s_add_u32 s2, s2, s4
	s_addc_u32 s3, s3, s5

	v_lshrrev_b32_e32 v2, 2, v66
	s_add_u32 s30, s2, 0x8000
	v_and_b32_e32 v2, 12, v2
	s_movk_i32 s9, 0xc0
	s_addc_u32 s31, s3, 0
	v_lshl_or_b32 v3, s37, 5, v2
	v_mul_lo_u32 v5, v66, s9
	s_add_i32 s8, 0, 0x10000

	v_add_u32_e32 v38, s8, v5
	v_mul_lo_u32 v5, v3, s9
	v_lshlrev_b32_e32 v2, 2, v2
	v_mov_b32_e32 v3, v87
	v_mov_b32_e32 v69, v87
	v_and_b32_e32 v1, 15, v66
	v_lshl_add_u64 v[26:27], s[0:1], 0, v[2:3]
	v_lshl_add_u64 v[2:3], s[6:7], 0, v[68:69]
	s_mov_b64 s[0:1], 0x5e10000
	v_lshl_add_u32 v4, v1, 2, 0
	v_lshl_add_u64 v[28:29], v[2:3], 0, s[0:1]
	s_movk_i32 s0, 0x600
	v_cmp_lt_i32_e64 s[2:3], 15, v66
	v_cmp_gt_u32_e64 s[4:5], 32, v66
	s_lshl_b32 s39, s36, 1
	v_cmp_gt_i32_e64 s[6:7], s0, v66
	v_lshl_add_u32 v39, v66, 2, 0
	v_add_u32_e32 v40, v4, v5
	s_branch .LBB0_3236
